# topk: batched affinity loads + register-resident binary search (on top of norm2/silu changes)
# speedup vs baseline: 1.0111x; 1.0111x over previous
; #define GAS __attribute__((address_space(1)))
; #define LAS __attribute__((address_space(3)))
; #define LDS_WAIT() asm volatile("s_waitcnt lgkmcnt(0)" ::: "memory")
; template <int NJ>
; __device__ __forceinline__ void topk_wave(Frame& F, const float* aff, int k, int srcrow0, int yrow0, int e, LAS unsigned* av) {
; #pragma unroll 1
;     for (int j = 0; j < NJ; ++j) av[j * 64 + F.lane] = __builtin_bit_cast(unsigned, *(const GAS float*)(aff + j * 64 + F.lane));
;     LDS_WAIT();
;     unsigned T = 0u;
; #pragma unroll 1
;     ...
; #pragma unroll 4
;         for (int j = 0; j < NJ; ++j) cnt += __popcll(__ballot(av[j * 64 + F.lane] >= cand));
;         if (cnt >= k) T = cand; }
.LBB0_977:
	s_lshr_b32 s16, s30, 4
	s_and_b32 s17, s36, 15
	s_lshl_b32 s41, s17, 2
	s_and_b32 s42, s16, 7
	s_mov_b64 s[16:17], -1
	s_and_b64 vcc, exec, s[0:1]
	s_cbranch_vccz .LBB0_991
	s_lshl_b32 s0, s30, 13
	s_and_b32 s20, s0, 0xfe000
	v_lshl_add_u64 v[8:9], v[4:5], 0, s[20:21]
	s_mov_b32 s0, 1
	s_mov_b32 s1, 0
	s_mov_b32 s16, 32
	v_add_co_u32_e32 v10, vcc, 0x1000, v8
	s_nop 1
	v_addc_co_u32_e32 v11, vcc, 0, v9, vcc
	global_load_dword v32, v[8:9], off
	global_load_dword v33, v[8:9], off offset:256
	global_load_dword v34, v[8:9], off offset:512
	global_load_dword v35, v[8:9], off offset:768
	global_load_dword v36, v[8:9], off offset:1024
	global_load_dword v37, v[8:9], off offset:1280
	global_load_dword v38, v[8:9], off offset:1536
	global_load_dword v39, v[8:9], off offset:1792
	global_load_dword v40, v[8:9], off offset:2048
	global_load_dword v41, v[8:9], off offset:2304
	global_load_dword v42, v[8:9], off offset:2560
	global_load_dword v43, v[8:9], off offset:2816
	global_load_dword v44, v[8:9], off offset:3072
	global_load_dword v45, v[8:9], off offset:3328
	global_load_dword v46, v[8:9], off offset:3584
	global_load_dword v47, v[8:9], off offset:3840
	global_load_dword v48, v[10:11], off
	global_load_dword v49, v[10:11], off offset:256
	global_load_dword v50, v[10:11], off offset:512
	global_load_dword v51, v[10:11], off offset:768
	global_load_dword v52, v[10:11], off offset:1024
	global_load_dword v53, v[10:11], off offset:1280
	global_load_dword v54, v[10:11], off offset:1536
	global_load_dword v55, v[10:11], off offset:1792
	global_load_dword v56, v[10:11], off offset:2048
	global_load_dword v57, v[10:11], off offset:2304
	global_load_dword v58, v[10:11], off offset:2560
	global_load_dword v59, v[10:11], off offset:2816
	global_load_dword v60, v[10:11], off offset:3072
	global_load_dword v61, v[10:11], off offset:3328
	global_load_dword v62, v[10:11], off offset:3584
	global_load_dword v63, v[10:11], off offset:3840
	s_waitcnt vmcnt(0)
	ds_write_b32 v12, v32
	ds_write_b32 v12, v33 offset:256
	ds_write_b32 v12, v34 offset:512
	ds_write_b32 v12, v35 offset:768
	ds_write_b32 v12, v36 offset:1024
	ds_write_b32 v12, v37 offset:1280
	ds_write_b32 v12, v38 offset:1536
	ds_write_b32 v12, v39 offset:1792
	ds_write_b32 v12, v40 offset:2048
	ds_write_b32 v12, v41 offset:2304
	ds_write_b32 v12, v42 offset:2560
	ds_write_b32 v12, v43 offset:2816
	ds_write_b32 v12, v44 offset:3072
	ds_write_b32 v12, v45 offset:3328
	ds_write_b32 v12, v46 offset:3584
	ds_write_b32 v12, v47 offset:3840
	ds_write_b32 v12, v48 offset:4096
	ds_write_b32 v12, v49 offset:4352
	ds_write_b32 v12, v50 offset:4608
	ds_write_b32 v12, v51 offset:4864
	ds_write_b32 v12, v52 offset:5120
	ds_write_b32 v12, v53 offset:5376
	ds_write_b32 v12, v54 offset:5632
	ds_write_b32 v12, v55 offset:5888
	ds_write_b32 v12, v56 offset:6144
	ds_write_b32 v12, v57 offset:6400
	ds_write_b32 v12, v58 offset:6656
	ds_write_b32 v12, v59 offset:6912
	ds_write_b32 v12, v60 offset:7168
	ds_write_b32 v12, v61 offset:7424
	ds_write_b32 v12, v62 offset:7680
	ds_write_b32 v12, v63 offset:7936
	s_waitcnt lgkmcnt(0)
	v_mov_b32_e32 v2, 30
	v_mov_b32_e32 v22, 0
.LBB0_981:
	v_lshlrev_b32_e64 v8, v2, 1
	v_or_b32_e32 v8, v8, v22
	s_mov_b32 s0, 0
	s_mov_b32 s1, 0
	v_cmp_ge_u32_e32 vcc, v32, v8
	v_cmp_ge_u32_e64 s[16:17], v33, v8
	v_cmp_ge_u32_e64 s[18:19], v34, v8
	v_cmp_ge_u32_e64 s[22:23], v35, v8
	s_bcnt1_i32_b64 s20, vcc
	s_bcnt1_i32_b64 s16, s[16:17]
	s_bcnt1_i32_b64 s17, s[18:19]
	s_bcnt1_i32_b64 s18, s[22:23]
	s_add_i32 s1, s1, s20
	s_add_i32 s1, s1, s16
	s_add_i32 s1, s1, s17
	s_add_i32 s1, s1, s18
	v_cmp_ge_u32_e32 vcc, v36, v8
	v_cmp_ge_u32_e64 s[16:17], v37, v8
	v_cmp_ge_u32_e64 s[18:19], v38, v8
	v_cmp_ge_u32_e64 s[22:23], v39, v8
	s_bcnt1_i32_b64 s20, vcc
	s_bcnt1_i32_b64 s16, s[16:17]
	s_bcnt1_i32_b64 s17, s[18:19]
	s_bcnt1_i32_b64 s18, s[22:23]
	s_add_i32 s1, s1, s20
	s_add_i32 s1, s1, s16
	s_add_i32 s1, s1, s17
	s_add_i32 s1, s1, s18
	v_cmp_ge_u32_e32 vcc, v40, v8
	v_cmp_ge_u32_e64 s[16:17], v41, v8
	v_cmp_ge_u32_e64 s[18:19], v42, v8
	v_cmp_ge_u32_e64 s[22:23], v43, v8
	s_bcnt1_i32_b64 s20, vcc
	s_bcnt1_i32_b64 s16, s[16:17]
	s_bcnt1_i32_b64 s17, s[18:19]
	s_bcnt1_i32_b64 s18, s[22:23]
	s_add_i32 s1, s1, s20
	s_add_i32 s1, s1, s16
	s_add_i32 s1, s1, s17
	s_add_i32 s1, s1, s18
	v_cmp_ge_u32_e32 vcc, v44, v8
	v_cmp_ge_u32_e64 s[16:17], v45, v8
	v_cmp_ge_u32_e64 s[18:19], v46, v8
	v_cmp_ge_u32_e64 s[22:23], v47, v8
	s_bcnt1_i32_b64 s20, vcc
	s_bcnt1_i32_b64 s16, s[16:17]
	s_bcnt1_i32_b64 s17, s[18:19]
	s_bcnt1_i32_b64 s18, s[22:23]
	s_add_i32 s1, s1, s20
	s_add_i32 s1, s1, s16
	s_add_i32 s1, s1, s17
	s_add_i32 s1, s1, s18
	v_cmp_ge_u32_e32 vcc, v48, v8
	v_cmp_ge_u32_e64 s[16:17], v49, v8
	v_cmp_ge_u32_e64 s[18:19], v50, v8
	v_cmp_ge_u32_e64 s[22:23], v51, v8
	s_bcnt1_i32_b64 s20, vcc
	s_bcnt1_i32_b64 s16, s[16:17]
	s_bcnt1_i32_b64 s17, s[18:19]
	s_bcnt1_i32_b64 s18, s[22:23]
	s_add_i32 s1, s1, s20
	s_add_i32 s1, s1, s16
	s_add_i32 s1, s1, s17
	s_add_i32 s1, s1, s18
	v_cmp_ge_u32_e32 vcc, v52, v8
	v_cmp_ge_u32_e64 s[16:17], v53, v8
	v_cmp_ge_u32_e64 s[18:19], v54, v8
	v_cmp_ge_u32_e64 s[22:23], v55, v8
	s_bcnt1_i32_b64 s20, vcc
	s_bcnt1_i32_b64 s16, s[16:17]
	s_bcnt1_i32_b64 s17, s[18:19]
	s_bcnt1_i32_b64 s18, s[22:23]
	s_add_i32 s1, s1, s20
	s_add_i32 s1, s1, s16
	s_add_i32 s1, s1, s17
	s_add_i32 s1, s1, s18
	v_cmp_ge_u32_e32 vcc, v56, v8
	v_cmp_ge_u32_e64 s[16:17], v57, v8
	v_cmp_ge_u32_e64 s[18:19], v58, v8
	v_cmp_ge_u32_e64 s[22:23], v59, v8
	s_bcnt1_i32_b64 s20, vcc
	s_bcnt1_i32_b64 s16, s[16:17]
	s_bcnt1_i32_b64 s17, s[18:19]
	s_bcnt1_i32_b64 s18, s[22:23]
	s_add_i32 s1, s1, s20
	s_add_i32 s1, s1, s16
	s_add_i32 s1, s1, s17
	s_add_i32 s1, s1, s18
	v_cmp_ge_u32_e32 vcc, v60, v8
	v_cmp_ge_u32_e64 s[16:17], v61, v8
	v_cmp_ge_u32_e64 s[18:19], v62, v8
	v_cmp_ge_u32_e64 s[22:23], v63, v8
	s_bcnt1_i32_b64 s20, vcc
	s_bcnt1_i32_b64 s16, s[16:17]
	s_bcnt1_i32_b64 s17, s[18:19]
	s_bcnt1_i32_b64 s18, s[22:23]
	s_add_i32 s1, s1, s20
	s_add_i32 s1, s1, s16
	s_add_i32 s1, s1, s17
	s_add_i32 s1, s1, s18
	s_cmpk_gt_i32 s1, 0xff
	s_cselect_b64 s[16:17], -1, 0
	v_subrev_co_u32_e32 v2, vcc, 1, v2
	s_andn2_b64 vcc, exec, vcc
	v_cndmask_b32_e64 v22, v22, v8, s[16:17]
	s_cbranch_vccnz .LBB0_981
	s_mov_b32 s0, 1
	v_mov_b32_e32 v2, 0
	s_mov_b32 s1, 32
	s_mov_b32 s20, 0
	v_mov_b32_e32 v8, 0
	v_mov_b32_e32 v9, 0
	v_mov_b32_e32 v10, 0

; #define GAS __attribute__((address_space(1)))
; #define LAS __attribute__((address_space(3)))
; #define LDS_WAIT() asm volatile("s_waitcnt lgkmcnt(0)" ::: "memory")
; template <int NJ>
; __device__ __forceinline__ void topk_wave(Frame& F, const float* aff, int k, int srcrow0, int yrow0, int e, LAS unsigned* av) {
; #pragma unroll 1
;     for (int j = 0; j < NJ; ++j) av[j * 64 + F.lane] = __builtin_bit_cast(unsigned, *(const GAS float*)(aff + j * 64 + F.lane));
;     LDS_WAIT();
;     unsigned T = 0u;
; #pragma unroll 1
;     ...
; #pragma unroll 4
;         for (int j = 0; j < NJ; ++j) cnt += __popcll(__ballot(av[j * 64 + F.lane] >= cand));
;         if (cnt >= k) T = cand; }
.LBB0_1990:
	s_lshl_b32 s0, s30, 13
	s_and_b32 s20, s0, 0xfe000
	v_lshl_add_u64 v[6:7], v[4:5], 0, s[20:21]
	s_mov_b32 s0, 32
	s_mov_b32 s1, s21
	s_mov_b32 s16, 1
	v_add_co_u32_e32 v8, vcc, 0x1000, v6
	s_nop 1
	v_addc_co_u32_e32 v9, vcc, 0, v7, vcc
	global_load_dword v32, v[6:7], off
	global_load_dword v33, v[6:7], off offset:256
	global_load_dword v34, v[6:7], off offset:512
	global_load_dword v35, v[6:7], off offset:768
	global_load_dword v36, v[6:7], off offset:1024
	global_load_dword v37, v[6:7], off offset:1280
	global_load_dword v38, v[6:7], off offset:1536
	global_load_dword v39, v[6:7], off offset:1792
	global_load_dword v40, v[6:7], off offset:2048
	global_load_dword v41, v[6:7], off offset:2304
	global_load_dword v42, v[6:7], off offset:2560
	global_load_dword v43, v[6:7], off offset:2816
	global_load_dword v44, v[6:7], off offset:3072
	global_load_dword v45, v[6:7], off offset:3328
	global_load_dword v46, v[6:7], off offset:3584
	global_load_dword v47, v[6:7], off offset:3840
	global_load_dword v48, v[8:9], off
	global_load_dword v49, v[8:9], off offset:256
	global_load_dword v50, v[8:9], off offset:512
	global_load_dword v51, v[8:9], off offset:768
	global_load_dword v52, v[8:9], off offset:1024
	global_load_dword v53, v[8:9], off offset:1280
	global_load_dword v54, v[8:9], off offset:1536
	global_load_dword v55, v[8:9], off offset:1792
	global_load_dword v56, v[8:9], off offset:2048
	global_load_dword v57, v[8:9], off offset:2304
	global_load_dword v58, v[8:9], off offset:2560
	global_load_dword v59, v[8:9], off offset:2816
	global_load_dword v60, v[8:9], off offset:3072
	global_load_dword v61, v[8:9], off offset:3328
	global_load_dword v62, v[8:9], off offset:3584
	global_load_dword v63, v[8:9], off offset:3840
	s_waitcnt vmcnt(0)
	ds_write_b32 v10, v32
	ds_write_b32 v10, v33 offset:256
	ds_write_b32 v10, v34 offset:512
	ds_write_b32 v10, v35 offset:768
	ds_write_b32 v10, v36 offset:1024
	ds_write_b32 v10, v37 offset:1280
	ds_write_b32 v10, v38 offset:1536
	ds_write_b32 v10, v39 offset:1792
	ds_write_b32 v10, v40 offset:2048
	ds_write_b32 v10, v41 offset:2304
	ds_write_b32 v10, v42 offset:2560
	ds_write_b32 v10, v43 offset:2816
	ds_write_b32 v10, v44 offset:3072
	ds_write_b32 v10, v45 offset:3328
	ds_write_b32 v10, v46 offset:3584
	ds_write_b32 v10, v47 offset:3840
	ds_write_b32 v10, v48 offset:4096
	ds_write_b32 v10, v49 offset:4352
	ds_write_b32 v10, v50 offset:4608
	ds_write_b32 v10, v51 offset:4864
	ds_write_b32 v10, v52 offset:5120
	ds_write_b32 v10, v53 offset:5376
	ds_write_b32 v10, v54 offset:5632
	ds_write_b32 v10, v55 offset:5888
	ds_write_b32 v10, v56 offset:6144
	ds_write_b32 v10, v57 offset:6400
	ds_write_b32 v10, v58 offset:6656
	ds_write_b32 v10, v59 offset:6912
	ds_write_b32 v10, v60 offset:7168
	ds_write_b32 v10, v61 offset:7424
	ds_write_b32 v10, v62 offset:7680
	ds_write_b32 v10, v63 offset:7936
	s_waitcnt lgkmcnt(0)
	v_mov_b32_e32 v2, 30
	v_mov_b32_e32 v19, 0
.LBB0_1993:
	v_lshlrev_b32_e64 v6, v2, 1
	v_or_b32_e32 v6, v6, v19
	s_mov_b32 s0, 0
	s_mov_b32 s1, 0
	v_cmp_ge_u32_e32 vcc, v32, v6
	v_cmp_ge_u32_e64 s[16:17], v33, v6
	v_cmp_ge_u32_e64 s[18:19], v34, v6
	v_cmp_ge_u32_e64 s[22:23], v35, v6
	s_bcnt1_i32_b64 s20, vcc
	s_bcnt1_i32_b64 s16, s[16:17]
	s_bcnt1_i32_b64 s17, s[18:19]
	s_bcnt1_i32_b64 s18, s[22:23]
	s_add_i32 s1, s1, s20
	s_add_i32 s1, s1, s16
	s_add_i32 s1, s1, s17
	s_add_i32 s1, s1, s18
	v_cmp_ge_u32_e32 vcc, v36, v6
	v_cmp_ge_u32_e64 s[16:17], v37, v6
	v_cmp_ge_u32_e64 s[18:19], v38, v6
	v_cmp_ge_u32_e64 s[22:23], v39, v6
	s_bcnt1_i32_b64 s20, vcc
	s_bcnt1_i32_b64 s16, s[16:17]
	s_bcnt1_i32_b64 s17, s[18:19]
	s_bcnt1_i32_b64 s18, s[22:23]
	s_add_i32 s1, s1, s20
	s_add_i32 s1, s1, s16
	s_add_i32 s1, s1, s17
	s_add_i32 s1, s1, s18
	v_cmp_ge_u32_e32 vcc, v40, v6
	v_cmp_ge_u32_e64 s[16:17], v41, v6
	v_cmp_ge_u32_e64 s[18:19], v42, v6
	v_cmp_ge_u32_e64 s[22:23], v43, v6
	s_bcnt1_i32_b64 s20, vcc
	s_bcnt1_i32_b64 s16, s[16:17]
	s_bcnt1_i32_b64 s17, s[18:19]
	s_bcnt1_i32_b64 s18, s[22:23]
	s_add_i32 s1, s1, s20
	s_add_i32 s1, s1, s16
	s_add_i32 s1, s1, s17
	s_add_i32 s1, s1, s18
	v_cmp_ge_u32_e32 vcc, v44, v6
	v_cmp_ge_u32_e64 s[16:17], v45, v6
	v_cmp_ge_u32_e64 s[18:19], v46, v6
	v_cmp_ge_u32_e64 s[22:23], v47, v6
	s_bcnt1_i32_b64 s20, vcc
	s_bcnt1_i32_b64 s16, s[16:17]
	s_bcnt1_i32_b64 s17, s[18:19]
	s_bcnt1_i32_b64 s18, s[22:23]
	s_add_i32 s1, s1, s20
	s_add_i32 s1, s1, s16
	s_add_i32 s1, s1, s17
	s_add_i32 s1, s1, s18
	v_cmp_ge_u32_e32 vcc, v48, v6
	v_cmp_ge_u32_e64 s[16:17], v49, v6
	v_cmp_ge_u32_e64 s[18:19], v50, v6
	v_cmp_ge_u32_e64 s[22:23], v51, v6
	s_bcnt1_i32_b64 s20, vcc
	s_bcnt1_i32_b64 s16, s[16:17]
	s_bcnt1_i32_b64 s17, s[18:19]
	s_bcnt1_i32_b64 s18, s[22:23]
	s_add_i32 s1, s1, s20
	s_add_i32 s1, s1, s16
	s_add_i32 s1, s1, s17
	s_add_i32 s1, s1, s18
	v_cmp_ge_u32_e32 vcc, v52, v6
	v_cmp_ge_u32_e64 s[16:17], v53, v6
	v_cmp_ge_u32_e64 s[18:19], v54, v6
	v_cmp_ge_u32_e64 s[22:23], v55, v6
	s_bcnt1_i32_b64 s20, vcc
	s_bcnt1_i32_b64 s16, s[16:17]
	s_bcnt1_i32_b64 s17, s[18:19]
	s_bcnt1_i32_b64 s18, s[22:23]
	s_add_i32 s1, s1, s20
	s_add_i32 s1, s1, s16
	s_add_i32 s1, s1, s17
	s_add_i32 s1, s1, s18
	v_cmp_ge_u32_e32 vcc, v56, v6
	v_cmp_ge_u32_e64 s[16:17], v57, v6
	v_cmp_ge_u32_e64 s[18:19], v58, v6
	v_cmp_ge_u32_e64 s[22:23], v59, v6
	s_bcnt1_i32_b64 s20, vcc
	s_bcnt1_i32_b64 s16, s[16:17]
	s_bcnt1_i32_b64 s17, s[18:19]
	s_bcnt1_i32_b64 s18, s[22:23]
	s_add_i32 s1, s1, s20
	s_add_i32 s1, s1, s16
	s_add_i32 s1, s1, s17
	s_add_i32 s1, s1, s18
	v_cmp_ge_u32_e32 vcc, v60, v6
	v_cmp_ge_u32_e64 s[16:17], v61, v6
	v_cmp_ge_u32_e64 s[18:19], v62, v6
	v_cmp_ge_u32_e64 s[22:23], v63, v6
	s_bcnt1_i32_b64 s20, vcc
	s_bcnt1_i32_b64 s16, s[16:17]
	s_bcnt1_i32_b64 s17, s[18:19]
	s_bcnt1_i32_b64 s18, s[22:23]
	s_add_i32 s1, s1, s20
	s_add_i32 s1, s1, s16
	s_add_i32 s1, s1, s17
	s_add_i32 s1, s1, s18
	s_cmpk_gt_i32 s1, 0xff
	s_cselect_b64 s[16:17], -1, 0
	v_subrev_co_u32_e32 v2, vcc, 1, v2
	s_andn2_b64 vcc, exec, vcc
	v_cndmask_b32_e64 v19, v19, v6, s[16:17]
	s_cbranch_vccnz .LBB0_1993
	s_mov_b32 s0, 1
	v_mov_b32_e32 v2, 0
	s_mov_b32 s1, 32
	s_mov_b32 s20, 0
	v_mov_b32_e32 v6, 0
	v_mov_b32_e32 v7, 0
	v_mov_b32_e32 v8, 0
